# speedup vs baseline: 1.0457x; 1.0204x over previous
_Z13attn11_kernelILi4EEvPc:
	s_ashr_i32 s5, s2, 3
	s_load_dwordx2 s[12:13], s[0:1], 0x0
	s_lshr_b32 s4, s5, 29
	s_lshl_b32 s3, s2, 4
	s_add_i32 s6, s5, s4
	s_and_b32 s3, s3, 0x70
	s_ashr_i32 s4, s6, 3
	s_add_i32 s4, s3, s4
	s_and_b32 s3, s6, 0x1fffff8
	s_sub_i32 s3, s5, s3
	v_lshrrev_b32_e32 v1, 6, v0
	s_waitcnt lgkmcnt(0)
	s_add_u32 s14, s12, 0x2500000
	v_lshlrev_b32_e32 v192, 5, v1
	s_addc_u32 s15, s13, 0
	s_ashr_i32 s5, s4, 31
	s_mul_i32 s6, s4, 0x12000
	v_lshl_or_b32 v172, s3, 7, v192
	s_mul_hi_i32 s3, s4, 0x12000
	s_add_u32 s8, s14, s6
	s_addc_u32 s9, s15, s3
	s_add_u32 s16, s12, 0x3700000
	v_lshlrev_b32_e32 v169, 4, v0
	s_addc_u32 s17, s13, 0
	s_add_u32 s10, s16, s6
	v_add_u32_e32 v193, 0, v169
	v_lshrrev_b32_e32 v2, 2, v0
	v_bitop3_b32 v3, v169, 48, v0 bitop3:0x48
	s_addc_u32 s11, s17, s3
	s_mov_b64 s[46:47], s[8:9]
	s_mov_b64 s[48:49], s[10:11]
	s_mov_b64 s[50:51], s[14:15]
	s_mov_b64 s[52:53], s[16:17]
	v_readfirstlane_b32 s3, v193
	v_add_u32_e32 v4, 0x8000, v193
	v_lshl_or_b32 v170, v2, 6, v3
	v_mul_u32_u24_e32 v2, 0x480, v2
	v_mov_b32_e32 v171, 0
	s_mov_b32 m0, s3
	v_readfirstlane_b32 s3, v4
	v_add_u32_e32 v6, 0x2000, v193
	v_or_b32_e32 v2, v2, v3
	v_lshl_add_u64 v[174:175], s[8:9], 0, v[170:171]
	v_mov_b32_e32 v3, v171
	global_load_lds_dwordx4 v170, s[8:9]
	v_mov_b32_e32 v220, v170
	s_mov_b32 m0, s3
	s_mov_b64 s[8:9], 0x1000
	v_readfirstlane_b32 s6, v6
	v_add_u32_e32 v6, 0x4000, v193
	v_lshl_add_u64 v[176:177], s[10:11], 0, v[2:3]
	global_load_lds_dwordx4 v2, s[10:11]
	v_mov_b32_e32 v221, v2
	v_lshl_add_u64 v[4:5], v[174:175], 0, s[8:9]
	s_mov_b32 m0, s6
	s_mov_b64 s[10:11], 0x2000
	v_readfirstlane_b32 s6, v6
	v_add_u32_e32 v6, 0xa000, v193
	global_load_lds_dwordx4 v[4:5], off
	v_lshl_add_u64 v[4:5], v[174:175], 0, s[10:11]
	s_mov_b32 m0, s6
	v_readfirstlane_b32 s6, v6
	s_add_u32 s18, s12, 0x1500000
	global_load_lds_dwordx4 v[4:5], off
	v_lshl_add_u64 v[4:5], v[176:177], 0, 64
	s_mov_b32 m0, s6
	s_addc_u32 s19, s13, 0
	s_lshl_b64 s[20:21], s[4:5], 10
	v_ashrrev_i32_e32 v173, 31, v172
	v_and_b32_e32 v168, 31, v0
	global_load_lds_dwordx4 v[4:5], off
	v_lshl_add_u64 v[4:5], s[20:21], 0, v[172:173]
	v_or_b32_e32 v4, v4, v168
	v_lshlrev_b64 v[4:5], 6, v[4:5]
	v_lshl_add_u64 v[4:5], s[18:19], 0, v[4:5]
	v_and_b32_e32 v6, 32, v0
	v_mov_b32_e32 v7, v171
	v_lshl_add_u64 v[4:5], v[4:5], 0, v[6:7]
	global_load_dwordx4 v[152:155], v[4:5], off
	global_load_dwordx4 v[156:159], v[4:5], off offset:16
	v_and_b32_e32 v4, 60, v0
	v_lshlrev_b32_e32 v5, 2, v0
	s_add_u32 s0, s0, 8
	s_movk_i32 s5, 0xa00
	v_lshlrev_b32_e32 v184, 7, v4
	v_or_b32_e32 v4, 64, v4
	v_bitop3_b32 v195, v5, v6, 48 bitop3:0x6c
	v_lshl_add_u64 v[178:179], s[14:15], 0, v[170:171]
	v_lshl_add_u64 v[180:181], s[16:17], 0, v[2:3]
	s_addc_u32 s1, s1, 0
	v_mad_u32_u24 v1, v1, s5, 0
	v_lshrrev_b32_e32 v2, 3, v0
	s_movk_i32 s5, 0x50
	v_and_b32_e32 v170, 48, v169
	v_bfe_u32 v0, v0, 2, 4
	v_lshrrev_b32_e32 v5, 2, v4
	v_mov_b32_e32 v144, 0x38383838
	v_bfe_u32 v226, v169, 6, 1
	v_bfe_u32 v227, v169, 8, 1
	v_cmp_eq_u32_e32 vcc, v226, v227
	s_nop 1
	v_cndmask_b32_e32 v144, 0, v144, vcc
	v_lshl_add_u64 v[182:183], s[18:19], 0, v[6:7]
	v_and_b32_e32 v2, 4, v2
	v_mad_u32_u24 v3, v168, s5, v1
	s_add_u32 s12, s12, 0x4900000
	v_add_u32_e32 v1, v1, v170
	v_mul_u32_u24_e32 v0, 0x50, v0
	v_mul_u32_u24_e32 v5, 0x50, v5
	s_movk_i32 s18, 0xffc0
	v_lshlrev_b32_e32 v199, 6, v168
	s_mov_b32 s7, 0
	s_movk_i32 s3, 0x2000
	s_movk_i32 s33, 0x4000
	v_mov_b32_e32 v173, 0x74747474
	v_mov_b32_e32 v194, 0x7f7f7f7f
	v_mov_b32_e32 v145, v144
	v_mov_b32_e32 v146, v144
	v_mov_b32_e32 v147, v144
	v_mov_b32_e32 v148, v144
	v_mov_b32_e32 v149, v144
	v_mov_b32_e32 v150, v144
	v_mov_b32_e32 v151, v144
	s_addc_u32 s13, s13, 0
	v_mov_b32_e32 v185, v171
	v_lshlrev_b32_e32 v186, 7, v4
	v_mov_b32_e32 v187, v171
	s_mov_b64 s[30:31], -1
	s_mov_b64 s[14:15], 0x3000
	s_mov_b64 s[16:17], 0xc0
	s_mov_b32 s19, -1
	s_mov_b32 s5, 0xff61b1e6
	s_mov_b32 s36, 0x41000000
	s_mov_b64 s[20:21], 0x80
	s_mov_b64 s[22:23], 0x11000
	s_mov_b64 s[24:25], 0x400
	s_mov_b64 s[26:27], 0x440
	s_mov_b32 s37, 0x42800000
	v_add_u32_e32 v196, v3, v2
	v_add_u32_e32 v197, v1, v0
	v_add_u32_e32 v198, v1, v5
	v_add_u32_e32 v197, 0x10000, v197
	v_add_u32_e32 v198, 0x10000, v198
	v_mov_b32_e32 v0, v171
	v_mov_b32_e32 v1, v171
	v_mov_b32_e32 v2, v171
	v_mov_b32_e32 v3, v171
	v_mov_b32_e32 v4, v171
	v_mov_b32_e32 v5, v171
	v_mov_b32_e32 v6, v171
	v_mov_b32_e32 v8, v171
	v_mov_b32_e32 v9, v171
	v_mov_b32_e32 v10, v171
	v_mov_b32_e32 v11, v171
	v_mov_b32_e32 v12, v171
	v_mov_b32_e32 v13, v171
	v_mov_b32_e32 v14, v171
	v_mov_b32_e32 v15, v171
	s_mov_b32 s38, 0
	v_mov_b32_e32 v160, v171
	v_mov_b32_e32 v161, v171
	v_mov_b32_e32 v162, v171
	v_mov_b32_e32 v163, v171
	v_mov_b32_e32 v164, v171
	v_mov_b32_e32 v165, v171
	v_mov_b32_e32 v166, v171
	v_mov_b32_e32 v167, v171
	v_xor_b32_e32 v200, 16, v195
	v_add_u32_e32 v201, 0, v199
	v_add_u32_e32 v222, v199, v195
	v_add_u32_e32 v223, v199, v200
	v_readfirstlane_b32 s40, v169
	v_add_u32_e32 v224, 0x8000, v222
	v_add_u32_e32 v225, 0x8000, v223
	v_mov_b32_e32 v202, 0x12000
	s_branch .LBB3_3

.LBB3_2:
	v_exp_f32_e32 v81, v112
	v_exp_f32_e32 v82, v113
	v_exp_f32_e32 v85, v116
	v_exp_f32_e32 v86, v117
	v_exp_f32_e32 v89, v120
	v_exp_f32_e32 v90, v121
	v_exp_f32_e32 v93, v124
	v_exp_f32_e32 v94, v125
	v_exp_f32_e32 v64, v64
	v_exp_f32_e32 v65, v65
	v_exp_f32_e32 v68, v68
	v_exp_f32_e32 v69, v69
	v_exp_f32_e32 v72, v72
	v_exp_f32_e32 v73, v73
	v_exp_f32_e32 v76, v76
	v_exp_f32_e32 v77, v77
	v_exp_f32_e32 v83, v114
	v_exp_f32_e32 v84, v115
	v_exp_f32_e32 v87, v118
	v_exp_f32_e32 v88, v119
	v_exp_f32_e32 v91, v122
	v_exp_f32_e32 v92, v123
	v_exp_f32_e32 v95, v126
	v_exp_f32_e32 v96, v127
	v_exp_f32_e32 v66, v66
	v_exp_f32_e32 v67, v67
	v_exp_f32_e32 v70, v70
	v_exp_f32_e32 v71, v71
	v_exp_f32_e32 v74, v74
	v_exp_f32_e32 v75, v75
	v_exp_f32_e32 v78, v78
	v_exp_f32_e32 v79, v79
	v_cvt_pk_fp8_f32 v160, v81, v82
	v_cvt_pk_fp8_f32 v161, v85, v86
	v_cvt_pk_fp8_f32 v162, v89, v90
	v_cvt_pk_fp8_f32 v163, v93, v94
	v_cvt_pk_fp8_f32 v164, v64, v65
	v_cvt_pk_fp8_f32 v165, v68, v69
	v_cvt_pk_fp8_f32 v166, v72, v73
	v_cvt_pk_fp8_f32 v167, v76, v77
	v_cvt_pk_fp8_f32 v160, v83, v84 op_sel:[0,0,1]
	v_cvt_pk_fp8_f32 v161, v87, v88 op_sel:[0,0,1]
	v_cvt_pk_fp8_f32 v162, v91, v92 op_sel:[0,0,1]
	v_cvt_pk_fp8_f32 v163, v95, v96 op_sel:[0,0,1]
	v_cvt_pk_fp8_f32 v164, v66, v67 op_sel:[0,0,1]
	v_cvt_pk_fp8_f32 v165, v70, v71 op_sel:[0,0,1]
	v_cvt_pk_fp8_f32 v166, v74, v75 op_sel:[0,0,1]
	v_cvt_pk_fp8_f32 v167, v78, v79 op_sel:[0,0,1]
	s_lshl_b32 s6, s4, 7
	s_and_b32 s6, s6, 0xfffffc00
	v_mfma_scale_f32_16x16x128_f8f6f4 v[48:51], v[144:151], v[160:167], v[48:51], v194, v194 op_sel_hi:[0,0,0]
	s_nop 15
	s_nop 3
	s_lshl_b32 s4, s4, 6
	v_mul_f32_e32 v48, 0x41800000, v48
	s_waitcnt lgkmcnt(0)
	v_mfma_scale_f32_32x32x64_f8f6f4 v[32:47], v[128:135], v[160:167], v[32:47], v194, v194 op_sel_hi:[0,0,0]
	v_div_scale_f32 v49, s[30:31], v48, v48, s37
	v_rcp_f32_e32 v66, v49
	s_mov_b64 s[30:31], 0
	v_fma_f32 v50, -v49, v66, 1.0
	v_fmac_f32_e32 v66, v50, v66
	v_div_scale_f32 v50, vcc, s37, v48, s37
	v_mul_f32_e32 v51, v50, v66
	v_fma_f32 v52, -v49, v51, v50
	v_fmac_f32_e32 v51, v52, v66
	v_fma_f32 v49, -v49, v51, v50
	v_div_fmas_f32 v49, v49, v66, v51
	v_mfma_scale_f32_32x32x64_f8f6f4 v[16:31], v[136:143], v[160:167], v[16:31], v194, v194 op_sel_hi:[0,0,0]
	v_div_fixup_f32 v48, v49, v48, s37
	s_nop 6
	v_mul_f32_e32 v32, v48, v32
	v_mul_f32_e32 v33, v48, v33
	v_mov_b32_e32 v49, 0
	v_cvt_pk_fp8_f32 v49, v32, v33
	v_mul_f32_e32 v32, v48, v34
	v_mul_f32_e32 v33, v48, v35
	s_and_b64 vcc, exec, s[28:29]
	v_cvt_pk_fp8_f32 v49, v32, v33 op_sel:[0,0,1]
	v_mov_b32_e32 v32, 0
	v_mov_b32_e32 v33, 0
	s_nop 1
	v_mul_f32_e32 v16, v48, v16
	v_mul_f32_e32 v17, v48, v17
	v_cvt_pk_fp8_f32 v32, v16, v17
	v_mul_f32_e32 v16, v48, v36
	v_mul_f32_e32 v17, v48, v37
	v_cvt_pk_fp8_f32 v33, v16, v17
	v_mul_f32_e32 v18, v48, v18
	v_mul_f32_e32 v19, v48, v19
	v_mul_f32_e32 v16, v48, v38
	v_mul_f32_e32 v17, v48, v39
	v_cvt_pk_fp8_f32 v32, v18, v19 op_sel:[0,0,1]
	v_cvt_pk_fp8_f32 v33, v16, v17 op_sel:[0,0,1]
	v_mul_f32_e32 v16, v48, v20
	v_mul_f32_e32 v17, v48, v21
	v_mov_b32_e32 v18, 0
	v_cvt_pk_fp8_f32 v18, v16, v17
	v_mul_f32_e32 v17, v48, v22
	v_mul_f32_e32 v19, v48, v23
	v_mov_b32_e32 v22, 0
	v_cvt_pk_fp8_f32 v18, v17, v19 op_sel:[0,0,1]
	v_mul_f32_e32 v17, v48, v40
	v_mul_f32_e32 v19, v48, v41
	v_cvt_pk_fp8_f32 v22, v17, v19
	v_mul_f32_e32 v17, v48, v24
	v_mul_f32_e32 v19, v48, v25
	v_mov_b32_e32 v23, 0
	v_cvt_pk_fp8_f32 v23, v17, v19
	v_mul_f32_e32 v17, v48, v26
	v_mul_f32_e32 v19, v48, v27
	v_mov_b32_e32 v24, 0
	v_cvt_pk_fp8_f32 v23, v17, v19 op_sel:[0,0,1]
	v_mul_f32_e32 v17, v48, v44
	v_mul_f32_e32 v19, v48, v45
	v_cvt_pk_fp8_f32 v24, v17, v19
	v_mul_f32_e32 v17, v48, v28
	v_mul_f32_e32 v19, v48, v29
	v_mov_b32_e32 v25, 0
	v_cvt_pk_fp8_f32 v25, v17, v19
	v_mul_f32_e32 v20, v48, v42
	v_mul_f32_e32 v21, v48, v43
	v_cvt_pk_fp8_f32 v22, v20, v21 op_sel:[0,0,1]
	v_mul_f32_e32 v20, v48, v46
	v_mul_f32_e32 v21, v48, v47
	v_cvt_pk_fp8_f32 v24, v20, v21 op_sel:[0,0,1]
	v_mul_f32_e32 v17, v48, v30
	v_mul_f32_e32 v19, v48, v31
	v_add_u32_e32 v16, 0x10000, v196
	v_cvt_pk_fp8_f32 v25, v17, v19 op_sel:[0,0,1]
	ds_write2_b32 v16, v49, v33 offset1:2
	ds_write2_b32 v16, v32, v18 offset0:8 offset1:10
	ds_write2_b32 v16, v22, v24 offset0:4 offset1:6
	ds_write2_b32 v16, v23, v25 offset0:12 offset1:14
	v_add_u32_e32 v16, s6, v172
	v_ashrrev_i32_e32 v17, 31, v16
	s_waitcnt lgkmcnt(0)
	v_lshlrev_b64 v[16:17], 9, v[16:17]
	v_lshl_add_u64 v[20:21], s[12:13], 0, v[16:17]
	s_and_b32 s6, s4, 0x1c0
	ds_read_b128 v[16:19], v197
	v_lshl_add_u64 v[24:25], v[20:21], 0, s[6:7]
	ds_read_b128 v[20:23], v198
	v_lshl_add_u64 v[24:25], v[24:25], 0, v[170:171]
	v_lshl_add_u64 v[26:27], v[24:25], 0, v[184:185]
	s_waitcnt lgkmcnt(0)
	global_store_dwordx4 v[26:27], v[16:19], off
	s_mov_b32 s4, s34
	v_mov_b32_e32 v172, v80
	v_lshl_add_u64 v[16:17], v[24:25], 0, v[186:187]
	global_store_dwordx4 v[16:17], v[20:23], off
	s_waitcnt lgkmcnt(0)
	s_cbranch_vccnz .LBB3_18

.Lat_loop:
	ds_read_b128 v[112:115], v222 offset:8192
	ds_read_b128 v[128:131], v222 offset:10240
	ds_read_b128 v[116:119], v223 offset:8192
	ds_read_b128 v[132:135], v223 offset:10240
	s_add_u32 m0, s40, 0x6000
	s_nop 0
	global_load_lds_dwordx4 v220, s[42:43]
	s_add_u32 s42, s42, 0x1000
	s_addc_u32 s43, s43, 0
	s_add_u32 m0, s40, 0x0
	s_nop 0
	global_load_lds_dwordx4 v220, s[42:43]
	s_add_u32 s42, s42, 0x1000
	s_addc_u32 s43, s43, 0
	s_setprio 1
	v_exp_f32_e32 v80, v80
	v_exp_f32_e32 v81, v81
	v_exp_f32_e32 v82, v82
	v_exp_f32_e32 v83, v83
	v_exp_f32_e32 v84, v84
	v_exp_f32_e32 v85, v85
	v_exp_f32_e32 v86, v86
	v_exp_f32_e32 v87, v87
	v_cvt_pk_fp8_f32 v160, v80, v81
	v_cvt_pk_fp8_f32 v161, v84, v85
	v_exp_f32_e32 v88, v88
	v_exp_f32_e32 v89, v89
	v_cvt_pk_fp8_f32 v160, v82, v83 op_sel:[0,0,1]
	v_cvt_pk_fp8_f32 v161, v86, v87 op_sel:[0,0,1]
	v_exp_f32_e32 v90, v90
	v_exp_f32_e32 v91, v91
	v_exp_f32_e32 v92, v92
	v_exp_f32_e32 v93, v93
	v_exp_f32_e32 v94, v94
	v_exp_f32_e32 v95, v95
	s_waitcnt lgkmcnt(0)
	v_mfma_scale_f32_32x32x64_f8f6f4 v[112:127], v[112:119], v[152:159], v[64:79], v173, v194 op_sel_hi:[0,0,0]
	s_setprio 0
	ds_read_b128 v[80:83], v224 offset:0
	ds_read_b128 v[212:215], v224 offset:2048
	ds_read_b128 v[84:87], v225 offset:0
	ds_read_b128 v[216:219], v225 offset:2048
	v_cvt_pk_fp8_f32 v162, v88, v89
	v_cvt_pk_fp8_f32 v163, v92, v93
	v_exp_f32_e32 v96, v96
	v_exp_f32_e32 v97, v97
	v_cvt_pk_fp8_f32 v162, v90, v91 op_sel:[0,0,1]
	v_cvt_pk_fp8_f32 v163, v94, v95 op_sel:[0,0,1]
	v_exp_f32_e32 v98, v98
	v_exp_f32_e32 v99, v99
	v_exp_f32_e32 v100, v100
	v_exp_f32_e32 v101, v101
	v_exp_f32_e32 v102, v102
	v_exp_f32_e32 v103, v103
	v_mfma_scale_f32_32x32x64_f8f6f4 v[128:143], v[128:135], v[152:159], v[64:79], v173, v194 op_sel_hi:[0,0,0]
	v_cvt_pk_fp8_f32 v164, v96, v97
	v_cvt_pk_fp8_f32 v165, v100, v101
	v_exp_f32_e32 v104, v104
	v_exp_f32_e32 v105, v105
	v_cvt_pk_fp8_f32 v164, v98, v99 op_sel:[0,0,1]
	v_cvt_pk_fp8_f32 v165, v102, v103 op_sel:[0,0,1]
	v_exp_f32_e32 v106, v106
	v_exp_f32_e32 v107, v107
	v_exp_f32_e32 v108, v108
	v_exp_f32_e32 v109, v109
	v_exp_f32_e32 v110, v110
	v_exp_f32_e32 v111, v111
	s_nop 0
	v_cvt_pk_fp8_f32 v166, v104, v105
	v_cvt_pk_fp8_f32 v167, v108, v109
	v_cvt_pk_fp8_f32 v166, v106, v107 op_sel:[0,0,1]
	v_cvt_pk_fp8_f32 v167, v110, v111 op_sel:[0,0,1]
	s_setprio 2
	s_waitcnt lgkmcnt(0)
	v_mfma_scale_f32_32x32x64_f8f6f4 v[32:47], v[80:87], v[160:167], v[32:47], v194, v194 op_sel_hi:[0,0,0]
	ds_read_b128 v[80:83], v222 offset:16384
	ds_read_b128 v[96:99], v222 offset:18432
	ds_read_b128 v[84:87], v223 offset:16384
	ds_read_b128 v[100:103], v223 offset:18432
	v_max3_f32 v227, v112, s5, v113
	v_max3_f32 v227, v227, v114, v115
	v_max3_f32 v227, v227, v116, v117
	v_max3_f32 v227, v227, v118, v119
	v_max3_f32 v227, v227, v120, v121
	v_max3_f32 v227, v227, v122, v123
	v_max3_f32 v227, v227, v124, v125
	v_max3_f32 v227, v227, v126, v127
	s_add_u32 s44, s44, 64
	s_addc_u32 s45, s45, 0
	s_add_u32 m0, s40, 0xc000
	s_nop 0
	global_load_lds_dwordx4 v221, s[44:45]
	v_mfma_scale_f32_32x32x64_f8f6f4 v[16:31], v[212:219], v[160:167], v[16:31], v194, v194 op_sel_hi:[0,0,0]
	v_max3_f32 v226, v128, s5, v129
	v_max3_f32 v226, v226, v130, v131
	v_max3_f32 v226, v226, v132, v133
	v_max3_f32 v226, v226, v134, v135
	v_max3_f32 v226, v226, v136, v137
	v_max3_f32 v226, v226, v138, v139
	v_max3_f32 v226, v226, v140, v141
	v_max3_f32 v226, v226, v142, v143
	s_add_u32 s44, s44, 64
	s_addc_u32 s45, s45, 0
	s_add_u32 m0, s40, 0xe000
	s_nop 0
	global_load_lds_dwordx4 v221, s[44:45]
	v_mfma_scale_f32_16x16x128_f8f6f4 v[48:51], v[144:151], v[160:167], v[48:51], v194, v194 op_sel_hi:[0,0,0]
	s_setprio 0
	v_max_f32_e32 v226, v227, v226
	v_cmp_lt_f32_e32 vcc, s36, v226
	s_cbranch_vccnz .Lat_rare_L1
.Lat_back_L1:
	s_setprio 1
	v_exp_f32_e32 v112, v112
	v_exp_f32_e32 v113, v113
	v_exp_f32_e32 v114, v114
	v_exp_f32_e32 v115, v115
	v_exp_f32_e32 v116, v116
	v_exp_f32_e32 v117, v117
	v_exp_f32_e32 v118, v118
	v_exp_f32_e32 v119, v119
	s_waitcnt lgkmcnt(0)
	v_mfma_scale_f32_32x32x64_f8f6f4 v[80:95], v[80:87], v[152:159], v[64:79], v173, v194 op_sel_hi:[0,0,0]
	v_cvt_pk_fp8_f32 v160, v112, v113
	v_cvt_pk_fp8_f32 v161, v116, v117
	v_exp_f32_e32 v120, v120
	v_exp_f32_e32 v121, v121
	v_cvt_pk_fp8_f32 v160, v114, v115 op_sel:[0,0,1]
	v_cvt_pk_fp8_f32 v161, v118, v119 op_sel:[0,0,1]
	v_exp_f32_e32 v122, v122
	v_exp_f32_e32 v123, v123
	v_exp_f32_e32 v124, v124
	v_exp_f32_e32 v125, v125
	v_exp_f32_e32 v126, v126
	v_exp_f32_e32 v127, v127
	s_setprio 0
	ds_read_b128 v[112:115], v224 offset:8192
	ds_read_b128 v[212:215], v224 offset:10240
	ds_read_b128 v[116:119], v225 offset:8192
	ds_read_b128 v[216:219], v225 offset:10240
	v_cvt_pk_fp8_f32 v162, v120, v121
	v_cvt_pk_fp8_f32 v163, v124, v125
	v_exp_f32_e32 v128, v128
	v_exp_f32_e32 v129, v129
	v_cvt_pk_fp8_f32 v162, v122, v123 op_sel:[0,0,1]
	v_cvt_pk_fp8_f32 v163, v126, v127 op_sel:[0,0,1]
	v_exp_f32_e32 v130, v130
	v_exp_f32_e32 v131, v131
	v_exp_f32_e32 v132, v132
	v_exp_f32_e32 v133, v133
	v_exp_f32_e32 v134, v134
	v_exp_f32_e32 v135, v135
	v_mfma_scale_f32_32x32x64_f8f6f4 v[96:111], v[96:103], v[152:159], v[64:79], v173, v194 op_sel_hi:[0,0,0]
	v_cvt_pk_fp8_f32 v164, v128, v129
	v_cvt_pk_fp8_f32 v165, v132, v133
	v_exp_f32_e32 v136, v136
	v_exp_f32_e32 v137, v137
	v_cvt_pk_fp8_f32 v164, v130, v131 op_sel:[0,0,1]
	v_cvt_pk_fp8_f32 v165, v134, v135 op_sel:[0,0,1]
	v_exp_f32_e32 v138, v138
	v_exp_f32_e32 v139, v139
	v_exp_f32_e32 v140, v140
	v_exp_f32_e32 v141, v141
	v_exp_f32_e32 v142, v142
	v_exp_f32_e32 v143, v143
	s_nop 0
	v_cvt_pk_fp8_f32 v166, v136, v137
	v_cvt_pk_fp8_f32 v167, v140, v141
	v_cvt_pk_fp8_f32 v166, v138, v139 op_sel:[0,0,1]
	v_cvt_pk_fp8_f32 v167, v142, v143 op_sel:[0,0,1]
	s_setprio 2
	s_waitcnt lgkmcnt(0)
	v_mfma_scale_f32_32x32x64_f8f6f4 v[32:47], v[112:119], v[160:167], v[32:47], v194, v194 op_sel_hi:[0,0,0]
	v_max3_f32 v227, v80, s5, v81
	v_max3_f32 v227, v227, v82, v83
	v_max3_f32 v227, v227, v84, v85
	v_max3_f32 v227, v227, v86, v87
	v_max3_f32 v227, v227, v88, v89
	v_max3_f32 v227, v227, v90, v91
	v_max3_f32 v227, v227, v92, v93
	v_max3_f32 v227, v227, v94, v95
	v_mfma_scale_f32_32x32x64_f8f6f4 v[16:31], v[212:219], v[160:167], v[16:31], v194, v194 op_sel_hi:[0,0,0]
	v_max3_f32 v226, v96, s5, v97
	v_max3_f32 v226, v226, v98, v99
	v_max3_f32 v226, v226, v100, v101
	v_max3_f32 v226, v226, v102, v103
	v_max3_f32 v226, v226, v104, v105
	v_max3_f32 v226, v226, v106, v107
	v_max3_f32 v226, v226, v108, v109
	v_max3_f32 v226, v226, v110, v111
	v_mfma_scale_f32_16x16x128_f8f6f4 v[48:51], v[144:151], v[160:167], v[48:51], v194, v194 op_sel_hi:[0,0,0]
	s_setprio 0
	v_max_f32_e32 v226, v227, v226
	v_cmp_lt_f32_e32 vcc, s36, v226
	s_cbranch_vccnz .Lat_rare_L2
.Lat_back_L2:
	s_waitcnt vmcnt(0) lgkmcnt(0)
	s_barrier
	ds_read_b128 v[112:115], v222 offset:24576
	ds_read_b128 v[128:131], v222 offset:26624
	ds_read_b128 v[116:119], v223 offset:24576
	ds_read_b128 v[132:135], v223 offset:26624
	s_add_u32 m0, s40, 0x2000
	s_nop 0
	global_load_lds_dwordx4 v220, s[42:43]
	s_add_u32 s42, s42, 0x1000
	s_addc_u32 s43, s43, 0
	s_add_u32 m0, s40, 0x4000
	s_nop 0
	global_load_lds_dwordx4 v220, s[42:43]
	s_add_u32 s42, s42, 0x1000
	s_addc_u32 s43, s43, 0
	s_setprio 1
	v_exp_f32_e32 v80, v80
	v_exp_f32_e32 v81, v81
	v_exp_f32_e32 v82, v82
	v_exp_f32_e32 v83, v83
	v_exp_f32_e32 v84, v84
	v_exp_f32_e32 v85, v85
	v_exp_f32_e32 v86, v86
	v_exp_f32_e32 v87, v87
	v_cvt_pk_fp8_f32 v160, v80, v81
	v_cvt_pk_fp8_f32 v161, v84, v85
	v_exp_f32_e32 v88, v88
	v_exp_f32_e32 v89, v89
	v_cvt_pk_fp8_f32 v160, v82, v83 op_sel:[0,0,1]
	v_cvt_pk_fp8_f32 v161, v86, v87 op_sel:[0,0,1]
	v_exp_f32_e32 v90, v90
	v_exp_f32_e32 v91, v91
	v_exp_f32_e32 v92, v92
	v_exp_f32_e32 v93, v93
	v_exp_f32_e32 v94, v94
	v_exp_f32_e32 v95, v95
	s_waitcnt lgkmcnt(0)
	v_mfma_scale_f32_32x32x64_f8f6f4 v[112:127], v[112:119], v[152:159], v[64:79], v173, v194 op_sel_hi:[0,0,0]
	s_setprio 0
	ds_read_b128 v[80:83], v224 offset:16384
	ds_read_b128 v[212:215], v224 offset:18432
	ds_read_b128 v[84:87], v225 offset:16384
	ds_read_b128 v[216:219], v225 offset:18432
	v_cvt_pk_fp8_f32 v162, v88, v89
	v_cvt_pk_fp8_f32 v163, v92, v93
	v_exp_f32_e32 v96, v96
	v_exp_f32_e32 v97, v97
	v_cvt_pk_fp8_f32 v162, v90, v91 op_sel:[0,0,1]
	v_cvt_pk_fp8_f32 v163, v94, v95 op_sel:[0,0,1]
	v_exp_f32_e32 v98, v98
	v_exp_f32_e32 v99, v99
	v_exp_f32_e32 v100, v100
	v_exp_f32_e32 v101, v101
	v_exp_f32_e32 v102, v102
	v_exp_f32_e32 v103, v103
	v_mfma_scale_f32_32x32x64_f8f6f4 v[128:143], v[128:135], v[152:159], v[64:79], v173, v194 op_sel_hi:[0,0,0]
	v_cvt_pk_fp8_f32 v164, v96, v97
	v_cvt_pk_fp8_f32 v165, v100, v101
	v_exp_f32_e32 v104, v104
	v_exp_f32_e32 v105, v105
	v_cvt_pk_fp8_f32 v164, v98, v99 op_sel:[0,0,1]
	v_cvt_pk_fp8_f32 v165, v102, v103 op_sel:[0,0,1]
	v_exp_f32_e32 v106, v106
	v_exp_f32_e32 v107, v107
	v_exp_f32_e32 v108, v108
	v_exp_f32_e32 v109, v109
	v_exp_f32_e32 v110, v110
	v_exp_f32_e32 v111, v111
	s_nop 0
	v_cvt_pk_fp8_f32 v166, v104, v105
	v_cvt_pk_fp8_f32 v167, v108, v109
	v_cvt_pk_fp8_f32 v166, v106, v107 op_sel:[0,0,1]
	v_cvt_pk_fp8_f32 v167, v110, v111 op_sel:[0,0,1]
	s_setprio 2
	s_waitcnt lgkmcnt(0)
	v_mfma_scale_f32_32x32x64_f8f6f4 v[32:47], v[80:87], v[160:167], v[32:47], v194, v194 op_sel_hi:[0,0,0]
	ds_read_b128 v[80:83], v222 offset:0
	ds_read_b128 v[96:99], v222 offset:2048
	ds_read_b128 v[84:87], v223 offset:0
	ds_read_b128 v[100:103], v223 offset:2048
	v_max3_f32 v227, v112, s5, v113
	v_max3_f32 v227, v227, v114, v115
	v_max3_f32 v227, v227, v116, v117
	v_max3_f32 v227, v227, v118, v119
	v_max3_f32 v227, v227, v120, v121
	v_max3_f32 v227, v227, v122, v123
	v_max3_f32 v227, v227, v124, v125
	v_max3_f32 v227, v227, v126, v127
	s_add_u32 s44, s44, 64
	s_addc_u32 s45, s45, 0
	s_add_u32 m0, s40, 0x8000
	s_nop 0
	global_load_lds_dwordx4 v221, s[44:45]
	v_mfma_scale_f32_32x32x64_f8f6f4 v[16:31], v[212:219], v[160:167], v[16:31], v194, v194 op_sel_hi:[0,0,0]
	v_max3_f32 v226, v128, s5, v129
	v_max3_f32 v226, v226, v130, v131
	v_max3_f32 v226, v226, v132, v133
	v_max3_f32 v226, v226, v134, v135
	v_max3_f32 v226, v226, v136, v137
	v_max3_f32 v226, v226, v138, v139
	v_max3_f32 v226, v226, v140, v141
	v_max3_f32 v226, v226, v142, v143
	s_add_u32 s44, s44, 64
	s_addc_u32 s45, s45, 0
	s_add_u32 m0, s40, 0xa000
	s_nop 0
	global_load_lds_dwordx4 v221, s[44:45]
	v_mfma_scale_f32_16x16x128_f8f6f4 v[48:51], v[144:151], v[160:167], v[48:51], v194, v194 op_sel_hi:[0,0,0]
	s_setprio 0
	v_max_f32_e32 v226, v227, v226
	v_cmp_lt_f32_e32 vcc, s36, v226
	s_cbranch_vccnz .Lat_rare_L3
.Lat_back_L3:
	s_setprio 1
	v_exp_f32_e32 v112, v112
	v_exp_f32_e32 v113, v113
	v_exp_f32_e32 v114, v114
	v_exp_f32_e32 v115, v115
	v_exp_f32_e32 v116, v116
	v_exp_f32_e32 v117, v117
	v_exp_f32_e32 v118, v118
	v_exp_f32_e32 v119, v119
	s_waitcnt lgkmcnt(0)
	v_mfma_scale_f32_32x32x64_f8f6f4 v[80:95], v[80:87], v[152:159], v[64:79], v173, v194 op_sel_hi:[0,0,0]
	v_cvt_pk_fp8_f32 v160, v112, v113
	v_cvt_pk_fp8_f32 v161, v116, v117
	v_exp_f32_e32 v120, v120
	v_exp_f32_e32 v121, v121
	v_cvt_pk_fp8_f32 v160, v114, v115 op_sel:[0,0,1]
	v_cvt_pk_fp8_f32 v161, v118, v119 op_sel:[0,0,1]
	v_exp_f32_e32 v122, v122
	v_exp_f32_e32 v123, v123
	v_exp_f32_e32 v124, v124
	v_exp_f32_e32 v125, v125
	v_exp_f32_e32 v126, v126
	v_exp_f32_e32 v127, v127
	s_setprio 0
	ds_read_b128 v[112:115], v224 offset:24576
	ds_read_b128 v[212:215], v224 offset:26624
	ds_read_b128 v[116:119], v225 offset:24576
	ds_read_b128 v[216:219], v225 offset:26624
	v_cvt_pk_fp8_f32 v162, v120, v121
	v_cvt_pk_fp8_f32 v163, v124, v125
	v_exp_f32_e32 v128, v128
	v_exp_f32_e32 v129, v129
	v_cvt_pk_fp8_f32 v162, v122, v123 op_sel:[0,0,1]
	v_cvt_pk_fp8_f32 v163, v126, v127 op_sel:[0,0,1]
	v_exp_f32_e32 v130, v130
	v_exp_f32_e32 v131, v131
	v_exp_f32_e32 v132, v132
	v_exp_f32_e32 v133, v133
	v_exp_f32_e32 v134, v134
	v_exp_f32_e32 v135, v135
	v_mfma_scale_f32_32x32x64_f8f6f4 v[96:111], v[96:103], v[152:159], v[64:79], v173, v194 op_sel_hi:[0,0,0]
	v_cvt_pk_fp8_f32 v164, v128, v129
	v_cvt_pk_fp8_f32 v165, v132, v133
	v_exp_f32_e32 v136, v136
	v_exp_f32_e32 v137, v137
	v_cvt_pk_fp8_f32 v164, v130, v131 op_sel:[0,0,1]
	v_cvt_pk_fp8_f32 v165, v134, v135 op_sel:[0,0,1]
	v_exp_f32_e32 v138, v138
	v_exp_f32_e32 v139, v139
	v_exp_f32_e32 v140, v140
	v_exp_f32_e32 v141, v141
	v_exp_f32_e32 v142, v142
	v_exp_f32_e32 v143, v143
	s_nop 0
	v_cvt_pk_fp8_f32 v166, v136, v137
	v_cvt_pk_fp8_f32 v167, v140, v141
	v_cvt_pk_fp8_f32 v166, v138, v139 op_sel:[0,0,1]
	v_cvt_pk_fp8_f32 v167, v142, v143 op_sel:[0,0,1]
	s_setprio 2
	s_waitcnt lgkmcnt(0)
	v_mfma_scale_f32_32x32x64_f8f6f4 v[32:47], v[112:119], v[160:167], v[32:47], v194, v194 op_sel_hi:[0,0,0]
	v_max3_f32 v227, v80, s5, v81
	v_max3_f32 v227, v227, v82, v83
	v_max3_f32 v227, v227, v84, v85
	v_max3_f32 v227, v227, v86, v87
	v_max3_f32 v227, v227, v88, v89
	v_max3_f32 v227, v227, v90, v91
	v_max3_f32 v227, v227, v92, v93
	v_max3_f32 v227, v227, v94, v95
	v_mfma_scale_f32_32x32x64_f8f6f4 v[16:31], v[212:219], v[160:167], v[16:31], v194, v194 op_sel_hi:[0,0,0]
	v_max3_f32 v226, v96, s5, v97
	v_max3_f32 v226, v226, v98, v99
	v_max3_f32 v226, v226, v100, v101
	v_max3_f32 v226, v226, v102, v103
	v_max3_f32 v226, v226, v104, v105
	v_max3_f32 v226, v226, v106, v107
	v_max3_f32 v226, v226, v108, v109
	v_max3_f32 v226, v226, v110, v111
	v_mfma_scale_f32_16x16x128_f8f6f4 v[48:51], v[144:151], v[160:167], v[48:51], v194, v194 op_sel_hi:[0,0,0]
	s_setprio 0
	v_max_f32_e32 v226, v227, v226
	v_cmp_lt_f32_e32 vcc, s36, v226
	s_cbranch_vccnz .Lat_rare_L4
.Lat_back_L4:
	s_waitcnt vmcnt(0) lgkmcnt(0)
	s_barrier
	s_add_u32 s39, s39, 1
	s_cmp_lt_u32 s39, 3
	s_cbranch_scc1 .Lat_loop
	ds_read_b128 v[112:115], v222 offset:8192
	ds_read_b128 v[128:131], v222 offset:10240
	ds_read_b128 v[116:119], v223 offset:8192
	ds_read_b128 v[132:135], v223 offset:10240
	s_add_u32 m0, s40, 0x6000
	s_nop 0
	global_load_lds_dwordx4 v220, s[42:43]
	s_add_u32 s42, s42, 0x1000
	s_addc_u32 s43, s43, 0
	s_add_u32 m0, s40, 0x0
	s_nop 0
	global_load_lds_dwordx4 v220, s[42:43]
	s_add_u32 s42, s42, 0x1000
	s_addc_u32 s43, s43, 0
	s_setprio 1
	v_exp_f32_e32 v80, v80
	v_exp_f32_e32 v81, v81
	v_exp_f32_e32 v82, v82
	v_exp_f32_e32 v83, v83
	v_exp_f32_e32 v84, v84
	v_exp_f32_e32 v85, v85
	v_exp_f32_e32 v86, v86
	v_exp_f32_e32 v87, v87
	v_cvt_pk_fp8_f32 v160, v80, v81
	v_cvt_pk_fp8_f32 v161, v84, v85
	v_exp_f32_e32 v88, v88
	v_exp_f32_e32 v89, v89
	v_cvt_pk_fp8_f32 v160, v82, v83 op_sel:[0,0,1]
	v_cvt_pk_fp8_f32 v161, v86, v87 op_sel:[0,0,1]
	v_exp_f32_e32 v90, v90
	v_exp_f32_e32 v91, v91
	v_exp_f32_e32 v92, v92
	v_exp_f32_e32 v93, v93
	v_exp_f32_e32 v94, v94
	v_exp_f32_e32 v95, v95
	s_waitcnt lgkmcnt(0)
	v_mfma_scale_f32_32x32x64_f8f6f4 v[112:127], v[112:119], v[152:159], v[64:79], v173, v194 op_sel_hi:[0,0,0]
	s_setprio 0
	ds_read_b128 v[80:83], v224 offset:0
	ds_read_b128 v[212:215], v224 offset:2048
	ds_read_b128 v[84:87], v225 offset:0
	ds_read_b128 v[216:219], v225 offset:2048
	v_cvt_pk_fp8_f32 v162, v88, v89
	v_cvt_pk_fp8_f32 v163, v92, v93
	v_exp_f32_e32 v96, v96
	v_exp_f32_e32 v97, v97
	v_cvt_pk_fp8_f32 v162, v90, v91 op_sel:[0,0,1]
	v_cvt_pk_fp8_f32 v163, v94, v95 op_sel:[0,0,1]
	v_exp_f32_e32 v98, v98
	v_exp_f32_e32 v99, v99
	v_exp_f32_e32 v100, v100
	v_exp_f32_e32 v101, v101
	v_exp_f32_e32 v102, v102
	v_exp_f32_e32 v103, v103
	v_mfma_scale_f32_32x32x64_f8f6f4 v[128:143], v[128:135], v[152:159], v[64:79], v173, v194 op_sel_hi:[0,0,0]
	v_cvt_pk_fp8_f32 v164, v96, v97
	v_cvt_pk_fp8_f32 v165, v100, v101
	v_exp_f32_e32 v104, v104
	v_exp_f32_e32 v105, v105
	v_cvt_pk_fp8_f32 v164, v98, v99 op_sel:[0,0,1]
	v_cvt_pk_fp8_f32 v165, v102, v103 op_sel:[0,0,1]
	v_exp_f32_e32 v106, v106
	v_exp_f32_e32 v107, v107
	v_exp_f32_e32 v108, v108
	v_exp_f32_e32 v109, v109
	v_exp_f32_e32 v110, v110
	v_exp_f32_e32 v111, v111
	s_nop 0
	v_cvt_pk_fp8_f32 v166, v104, v105
	v_cvt_pk_fp8_f32 v167, v108, v109
	v_cvt_pk_fp8_f32 v166, v106, v107 op_sel:[0,0,1]
	v_cvt_pk_fp8_f32 v167, v110, v111 op_sel:[0,0,1]
	s_setprio 2
	s_waitcnt lgkmcnt(0)
	v_mfma_scale_f32_32x32x64_f8f6f4 v[32:47], v[80:87], v[160:167], v[32:47], v194, v194 op_sel_hi:[0,0,0]
	ds_read_b128 v[80:83], v222 offset:16384
	ds_read_b128 v[96:99], v222 offset:18432
	ds_read_b128 v[84:87], v223 offset:16384
	ds_read_b128 v[100:103], v223 offset:18432
	v_max3_f32 v227, v112, s5, v113
	v_max3_f32 v227, v227, v114, v115
	v_max3_f32 v227, v227, v116, v117
	v_max3_f32 v227, v227, v118, v119
	v_max3_f32 v227, v227, v120, v121
	v_max3_f32 v227, v227, v122, v123
	v_max3_f32 v227, v227, v124, v125
	v_max3_f32 v227, v227, v126, v127
	s_add_u32 s44, s44, 64
	s_addc_u32 s45, s45, 0
	s_add_u32 m0, s40, 0xc000
	s_nop 0
	global_load_lds_dwordx4 v221, s[44:45]
	v_mfma_scale_f32_32x32x64_f8f6f4 v[16:31], v[212:219], v[160:167], v[16:31], v194, v194 op_sel_hi:[0,0,0]
	v_max3_f32 v226, v128, s5, v129
	v_max3_f32 v226, v226, v130, v131
	v_max3_f32 v226, v226, v132, v133
	v_max3_f32 v226, v226, v134, v135
	v_max3_f32 v226, v226, v136, v137
	v_max3_f32 v226, v226, v138, v139
	v_max3_f32 v226, v226, v140, v141
	v_max3_f32 v226, v226, v142, v143
	s_add_u32 s44, s44, 64
	s_addc_u32 s45, s45, 0
	s_add_u32 m0, s40, 0xe000
	s_nop 0
	global_load_lds_dwordx4 v221, s[44:45]
	v_mfma_scale_f32_16x16x128_f8f6f4 v[48:51], v[144:151], v[160:167], v[48:51], v194, v194 op_sel_hi:[0,0,0]
	s_setprio 0
	v_max_f32_e32 v226, v227, v226
	v_cmp_lt_f32_e32 vcc, s36, v226
	s_cbranch_vccnz .Lat_rare_P13

.Lat_back_P14:
	s_waitcnt vmcnt(0) lgkmcnt(0)
	s_barrier
	ds_read_b128 v[112:115], v222 offset:24576
	ds_read_b128 v[128:131], v222 offset:26624
	ds_read_b128 v[116:119], v223 offset:24576
	ds_read_b128 v[132:135], v223 offset:26624
	s_add_u32 m0, s40, 0x2000
	s_nop 0
	global_load_lds_dwordx4 v220, s[42:43]
	s_add_u32 s42, s42, 0x1000
	s_addc_u32 s43, s43, 0
	s_setprio 1
	v_exp_f32_e32 v80, v80
	v_exp_f32_e32 v81, v81
	v_exp_f32_e32 v82, v82
	v_exp_f32_e32 v83, v83
	v_exp_f32_e32 v84, v84
	v_exp_f32_e32 v85, v85
	v_exp_f32_e32 v86, v86
	v_exp_f32_e32 v87, v87
	v_cvt_pk_fp8_f32 v160, v80, v81
	v_cvt_pk_fp8_f32 v161, v84, v85
	v_exp_f32_e32 v88, v88
	v_exp_f32_e32 v89, v89
	v_cvt_pk_fp8_f32 v160, v82, v83 op_sel:[0,0,1]
	v_cvt_pk_fp8_f32 v161, v86, v87 op_sel:[0,0,1]
	v_exp_f32_e32 v90, v90
	v_exp_f32_e32 v91, v91
	v_exp_f32_e32 v92, v92
	v_exp_f32_e32 v93, v93
	v_exp_f32_e32 v94, v94
	v_exp_f32_e32 v95, v95
	s_waitcnt lgkmcnt(0)
	v_mfma_scale_f32_32x32x64_f8f6f4 v[112:127], v[112:119], v[152:159], v[64:79], v173, v194 op_sel_hi:[0,0,0]
	s_setprio 0
	ds_read_b128 v[80:83], v224 offset:16384
	ds_read_b128 v[212:215], v224 offset:18432
	ds_read_b128 v[84:87], v225 offset:16384
	ds_read_b128 v[216:219], v225 offset:18432
	v_cvt_pk_fp8_f32 v162, v88, v89
	v_cvt_pk_fp8_f32 v163, v92, v93
	v_exp_f32_e32 v96, v96
	v_exp_f32_e32 v97, v97
	v_cvt_pk_fp8_f32 v162, v90, v91 op_sel:[0,0,1]
	v_cvt_pk_fp8_f32 v163, v94, v95 op_sel:[0,0,1]
	v_exp_f32_e32 v98, v98
	v_exp_f32_e32 v99, v99
	v_exp_f32_e32 v100, v100
	v_exp_f32_e32 v101, v101
	v_exp_f32_e32 v102, v102
	v_exp_f32_e32 v103, v103
	v_mfma_scale_f32_32x32x64_f8f6f4 v[128:143], v[128:135], v[152:159], v[64:79], v173, v194 op_sel_hi:[0,0,0]
	v_cvt_pk_fp8_f32 v164, v96, v97
	v_cvt_pk_fp8_f32 v165, v100, v101
	v_exp_f32_e32 v104, v104
	v_exp_f32_e32 v105, v105
	v_cvt_pk_fp8_f32 v164, v98, v99 op_sel:[0,0,1]
	v_cvt_pk_fp8_f32 v165, v102, v103 op_sel:[0,0,1]
	v_exp_f32_e32 v106, v106
	v_exp_f32_e32 v107, v107
	v_exp_f32_e32 v108, v108
	v_exp_f32_e32 v109, v109
	v_exp_f32_e32 v110, v110
	v_exp_f32_e32 v111, v111
	s_nop 0
	v_cvt_pk_fp8_f32 v166, v104, v105
	v_cvt_pk_fp8_f32 v167, v108, v109
	v_cvt_pk_fp8_f32 v166, v106, v107 op_sel:[0,0,1]
	v_cvt_pk_fp8_f32 v167, v110, v111 op_sel:[0,0,1]
	s_setprio 2
	s_waitcnt lgkmcnt(0)
	v_mfma_scale_f32_32x32x64_f8f6f4 v[32:47], v[80:87], v[160:167], v[32:47], v194, v194 op_sel_hi:[0,0,0]
	ds_read_b128 v[80:83], v222 offset:0
	ds_read_b128 v[96:99], v222 offset:2048
	ds_read_b128 v[84:87], v223 offset:0
	ds_read_b128 v[100:103], v223 offset:2048
	v_max3_f32 v227, v112, s5, v113
	v_max3_f32 v227, v227, v114, v115
	v_max3_f32 v227, v227, v116, v117
	v_max3_f32 v227, v227, v118, v119
	v_max3_f32 v227, v227, v120, v121
	v_max3_f32 v227, v227, v122, v123
	v_max3_f32 v227, v227, v124, v125
	v_max3_f32 v227, v227, v126, v127
	s_add_u32 s44, s44, 64
	s_addc_u32 s45, s45, 0
	s_add_u32 m0, s40, 0x8000
	s_nop 0
	global_load_lds_dwordx4 v221, s[44:45]
	v_mfma_scale_f32_32x32x64_f8f6f4 v[16:31], v[212:219], v[160:167], v[16:31], v194, v194 op_sel_hi:[0,0,0]
	v_max3_f32 v226, v128, s5, v129
	v_max3_f32 v226, v226, v130, v131
	v_max3_f32 v226, v226, v132, v133
	v_max3_f32 v226, v226, v134, v135
	v_max3_f32 v226, v226, v136, v137
	v_max3_f32 v226, v226, v138, v139
	v_max3_f32 v226, v226, v140, v141
	v_max3_f32 v226, v226, v142, v143
	s_add_u32 s44, s44, 64
	s_addc_u32 s45, s45, 0
	s_add_u32 m0, s40, 0xa000
	s_nop 0
	global_load_lds_dwordx4 v221, s[44:45]
	v_mfma_scale_f32_16x16x128_f8f6f4 v[48:51], v[144:151], v[160:167], v[48:51], v194, v194 op_sel_hi:[0,0,0]
	s_setprio 0
	v_max_f32_e32 v226, v227, v226
	v_cmp_lt_f32_e32 vcc, s36, v226
	s_cbranch_vccnz .Lat_rare_P15

.Lat_back_P16:
	s_waitcnt vmcnt(0) lgkmcnt(0)
	s_barrier
	ds_read_b128 v[112:115], v222 offset:8192
	ds_read_b128 v[128:131], v222 offset:10240
	ds_read_b128 v[116:119], v223 offset:8192
	ds_read_b128 v[132:135], v223 offset:10240
	s_setprio 1
	v_exp_f32_e32 v80, v80
	v_exp_f32_e32 v81, v81
	v_exp_f32_e32 v82, v82
	v_exp_f32_e32 v83, v83
	v_exp_f32_e32 v84, v84
	v_exp_f32_e32 v85, v85
	v_exp_f32_e32 v86, v86
	v_exp_f32_e32 v87, v87
	v_cvt_pk_fp8_f32 v160, v80, v81
	v_cvt_pk_fp8_f32 v161, v84, v85
	v_exp_f32_e32 v88, v88
	v_exp_f32_e32 v89, v89
	v_cvt_pk_fp8_f32 v160, v82, v83 op_sel:[0,0,1]
	v_cvt_pk_fp8_f32 v161, v86, v87 op_sel:[0,0,1]
	v_exp_f32_e32 v90, v90
	v_exp_f32_e32 v91, v91
	v_exp_f32_e32 v92, v92
	v_exp_f32_e32 v93, v93
	v_exp_f32_e32 v94, v94
	v_exp_f32_e32 v95, v95
	s_waitcnt lgkmcnt(0)
	v_mfma_scale_f32_32x32x64_f8f6f4 v[112:127], v[112:119], v[152:159], v[64:79], v173, v194 op_sel_hi:[0,0,0]
	s_setprio 0
	ds_read_b128 v[80:83], v224 offset:0
	ds_read_b128 v[136:139], v224 offset:2048
	ds_read_b128 v[84:87], v225 offset:0
	ds_read_b128 v[140:143], v225 offset:2048
	v_cvt_pk_fp8_f32 v162, v88, v89
	v_cvt_pk_fp8_f32 v163, v92, v93
	v_exp_f32_e32 v96, v96
	v_exp_f32_e32 v97, v97
	v_cvt_pk_fp8_f32 v162, v90, v91 op_sel:[0,0,1]
	v_cvt_pk_fp8_f32 v163, v94, v95 op_sel:[0,0,1]
	v_exp_f32_e32 v98, v98
	v_exp_f32_e32 v99, v99
	v_exp_f32_e32 v100, v100
	v_exp_f32_e32 v101, v101
	v_exp_f32_e32 v102, v102
	v_exp_f32_e32 v103, v103
	v_mfma_scale_f32_32x32x64_f8f6f4 v[64:79], v[128:135], v[152:159], v[64:79], v173, v194 op_sel_hi:[0,0,0]
	v_cvt_pk_fp8_f32 v164, v96, v97
	v_cvt_pk_fp8_f32 v165, v100, v101
	v_exp_f32_e32 v104, v104
	v_exp_f32_e32 v105, v105
	v_cvt_pk_fp8_f32 v164, v98, v99 op_sel:[0,0,1]
	v_cvt_pk_fp8_f32 v165, v102, v103 op_sel:[0,0,1]
	v_exp_f32_e32 v106, v106
	v_exp_f32_e32 v107, v107
	v_exp_f32_e32 v108, v108
	v_exp_f32_e32 v109, v109
	v_exp_f32_e32 v110, v110
	v_exp_f32_e32 v111, v111
	s_nop 0
	v_cvt_pk_fp8_f32 v166, v104, v105
	v_cvt_pk_fp8_f32 v167, v108, v109
	v_cvt_pk_fp8_f32 v166, v106, v107 op_sel:[0,0,1]
	v_cvt_pk_fp8_f32 v167, v110, v111 op_sel:[0,0,1]
	s_setprio 2
	s_waitcnt lgkmcnt(0)
	v_mfma_scale_f32_32x32x64_f8f6f4 v[32:47], v[80:87], v[160:167], v[32:47], v194, v194 op_sel_hi:[0,0,0]
	v_max3_f32 v227, v112, s5, v113
	v_max3_f32 v227, v227, v114, v115
	v_max3_f32 v227, v227, v116, v117
	v_max3_f32 v227, v227, v118, v119
	v_max3_f32 v227, v227, v120, v121
	v_max3_f32 v227, v227, v122, v123
	v_max3_f32 v227, v227, v124, v125
	v_max3_f32 v227, v227, v126, v127
	v_mfma_scale_f32_32x32x64_f8f6f4 v[16:31], v[136:143], v[160:167], v[16:31], v194, v194 op_sel_hi:[0,0,0]
	v_max3_f32 v226, v64, s5, v65
	v_max3_f32 v226, v226, v66, v67
	v_max3_f32 v226, v226, v68, v69
	v_max3_f32 v226, v226, v70, v71
	v_max3_f32 v226, v226, v72, v73
	v_max3_f32 v226, v226, v74, v75
	v_max3_f32 v226, v226, v76, v77
	v_max3_f32 v226, v226, v78, v79
	v_mfma_scale_f32_16x16x128_f8f6f4 v[48:51], v[144:151], v[160:167], v[48:51], v194, v194 op_sel_hi:[0,0,0]
	s_setprio 0
	v_max_f32_e32 v226, v227, v226
	v_cmp_lt_f32_e32 vcc, s36, v226
	s_cbranch_vccnz .Lat_rare_P17

.Lat_rare_L1:
	v_mov_b32_e32 v227, v226
	s_nop 1
	v_permlane32_swap_b32_e32 v226, v227
	v_max_f32_e32 v226, v226, v227
	v_max_f32_e32 v226, v226, v226
	v_max_f32_e32 v227, 0, v226
	v_exp_f32_e64 v226, -v227
	v_sub_f32_e32 v79, v79, v227
	v_sub_f32_e32 v78, v78, v227
	v_sub_f32_e32 v77, v77, v227
	v_sub_f32_e32 v76, v76, v227
	v_sub_f32_e32 v75, v75, v227
	v_sub_f32_e32 v74, v74, v227
	v_sub_f32_e32 v73, v73, v227
	v_sub_f32_e32 v72, v72, v227
	v_sub_f32_e32 v71, v71, v227
	v_sub_f32_e32 v70, v70, v227
	v_sub_f32_e32 v69, v69, v227
	v_sub_f32_e32 v68, v68, v227
	v_sub_f32_e32 v67, v67, v227
	v_sub_f32_e32 v66, v66, v227
	v_sub_f32_e32 v65, v65, v227
	v_sub_f32_e32 v64, v64, v227
	v_sub_f32_e32 v127, v127, v227
	v_sub_f32_e32 v126, v126, v227
	v_sub_f32_e32 v125, v125, v227
	v_sub_f32_e32 v124, v124, v227
	v_sub_f32_e32 v123, v123, v227
	v_sub_f32_e32 v122, v122, v227
	v_sub_f32_e32 v121, v121, v227
	v_sub_f32_e32 v120, v120, v227
	v_sub_f32_e32 v119, v119, v227
	v_sub_f32_e32 v118, v118, v227
	v_sub_f32_e32 v117, v117, v227
	v_sub_f32_e32 v116, v116, v227
	v_sub_f32_e32 v115, v115, v227
	v_sub_f32_e32 v114, v114, v227
	v_sub_f32_e32 v113, v113, v227
	v_sub_f32_e32 v112, v112, v227
	v_sub_f32_e32 v143, v143, v227
	v_sub_f32_e32 v142, v142, v227
	v_sub_f32_e32 v141, v141, v227
	v_sub_f32_e32 v140, v140, v227
	v_sub_f32_e32 v139, v139, v227
	v_sub_f32_e32 v138, v138, v227
	v_sub_f32_e32 v137, v137, v227
	v_sub_f32_e32 v136, v136, v227
	v_sub_f32_e32 v135, v135, v227
	v_sub_f32_e32 v134, v134, v227
	v_sub_f32_e32 v133, v133, v227
	v_sub_f32_e32 v132, v132, v227
	v_sub_f32_e32 v131, v131, v227
	v_sub_f32_e32 v130, v130, v227
	v_sub_f32_e32 v129, v129, v227
	v_sub_f32_e32 v128, v128, v227
	v_pk_mul_f32 v[46:47], v[226:227], v[46:47] op_sel_hi:[0,1]
	v_pk_mul_f32 v[44:45], v[226:227], v[44:45] op_sel_hi:[0,1]
	v_pk_mul_f32 v[42:43], v[226:227], v[42:43] op_sel_hi:[0,1]
	v_pk_mul_f32 v[40:41], v[226:227], v[40:41] op_sel_hi:[0,1]
	v_pk_mul_f32 v[38:39], v[226:227], v[38:39] op_sel_hi:[0,1]
	v_pk_mul_f32 v[36:37], v[226:227], v[36:37] op_sel_hi:[0,1]
	v_pk_mul_f32 v[34:35], v[226:227], v[34:35] op_sel_hi:[0,1]
	v_pk_mul_f32 v[32:33], v[226:227], v[32:33] op_sel_hi:[0,1]
	v_pk_mul_f32 v[30:31], v[226:227], v[30:31] op_sel_hi:[0,1]
	v_pk_mul_f32 v[28:29], v[226:227], v[28:29] op_sel_hi:[0,1]
	v_pk_mul_f32 v[26:27], v[226:227], v[26:27] op_sel_hi:[0,1]
	v_pk_mul_f32 v[24:25], v[226:227], v[24:25] op_sel_hi:[0,1]
	v_pk_mul_f32 v[22:23], v[226:227], v[22:23] op_sel_hi:[0,1]
	v_pk_mul_f32 v[20:21], v[226:227], v[20:21] op_sel_hi:[0,1]
	v_pk_mul_f32 v[18:19], v[226:227], v[18:19] op_sel_hi:[0,1]
	v_pk_mul_f32 v[16:17], v[226:227], v[16:17] op_sel_hi:[0,1]
	v_pk_mul_f32 v[50:51], v[226:227], v[50:51] op_sel_hi:[0,1]
	v_pk_mul_f32 v[48:49], v[226:227], v[48:49] op_sel_hi:[0,1]
	s_branch .Lat_back_L1
.Lat_rare_L2:
	v_mov_b32_e32 v227, v226
	s_nop 1
	v_permlane32_swap_b32_e32 v226, v227
	v_max_f32_e32 v226, v226, v227
	v_max_f32_e32 v226, v226, v226
	v_max_f32_e32 v227, 0, v226
	v_exp_f32_e64 v226, -v227
	v_sub_f32_e32 v79, v79, v227
	v_sub_f32_e32 v78, v78, v227
	v_sub_f32_e32 v77, v77, v227
	v_sub_f32_e32 v76, v76, v227
	v_sub_f32_e32 v75, v75, v227
	v_sub_f32_e32 v74, v74, v227
	v_sub_f32_e32 v73, v73, v227
	v_sub_f32_e32 v72, v72, v227
	v_sub_f32_e32 v71, v71, v227
	v_sub_f32_e32 v70, v70, v227
	v_sub_f32_e32 v69, v69, v227
	v_sub_f32_e32 v68, v68, v227
	v_sub_f32_e32 v67, v67, v227
	v_sub_f32_e32 v66, v66, v227
	v_sub_f32_e32 v65, v65, v227
	v_sub_f32_e32 v64, v64, v227
	v_sub_f32_e32 v95, v95, v227
	v_sub_f32_e32 v94, v94, v227
	v_sub_f32_e32 v93, v93, v227
	v_sub_f32_e32 v92, v92, v227
	v_sub_f32_e32 v91, v91, v227
	v_sub_f32_e32 v90, v90, v227
	v_sub_f32_e32 v89, v89, v227
	v_sub_f32_e32 v88, v88, v227
	v_sub_f32_e32 v87, v87, v227
	v_sub_f32_e32 v86, v86, v227
	v_sub_f32_e32 v85, v85, v227
	v_sub_f32_e32 v84, v84, v227
	v_sub_f32_e32 v83, v83, v227
	v_sub_f32_e32 v82, v82, v227
	v_sub_f32_e32 v81, v81, v227
	v_sub_f32_e32 v80, v80, v227
	v_sub_f32_e32 v111, v111, v227
	v_sub_f32_e32 v110, v110, v227
	v_sub_f32_e32 v109, v109, v227
	v_sub_f32_e32 v108, v108, v227
	v_sub_f32_e32 v107, v107, v227
	v_sub_f32_e32 v106, v106, v227
	v_sub_f32_e32 v105, v105, v227
	v_sub_f32_e32 v104, v104, v227
	v_sub_f32_e32 v103, v103, v227
	v_sub_f32_e32 v102, v102, v227
	v_sub_f32_e32 v101, v101, v227
	v_sub_f32_e32 v100, v100, v227
	v_sub_f32_e32 v99, v99, v227
	v_sub_f32_e32 v98, v98, v227
	v_sub_f32_e32 v97, v97, v227
	v_sub_f32_e32 v96, v96, v227
	v_pk_mul_f32 v[46:47], v[226:227], v[46:47] op_sel_hi:[0,1]
	v_pk_mul_f32 v[44:45], v[226:227], v[44:45] op_sel_hi:[0,1]
	v_pk_mul_f32 v[42:43], v[226:227], v[42:43] op_sel_hi:[0,1]
	v_pk_mul_f32 v[40:41], v[226:227], v[40:41] op_sel_hi:[0,1]
	v_pk_mul_f32 v[38:39], v[226:227], v[38:39] op_sel_hi:[0,1]
	v_pk_mul_f32 v[36:37], v[226:227], v[36:37] op_sel_hi:[0,1]
	v_pk_mul_f32 v[34:35], v[226:227], v[34:35] op_sel_hi:[0,1]
	v_pk_mul_f32 v[32:33], v[226:227], v[32:33] op_sel_hi:[0,1]
	v_pk_mul_f32 v[30:31], v[226:227], v[30:31] op_sel_hi:[0,1]
	v_pk_mul_f32 v[28:29], v[226:227], v[28:29] op_sel_hi:[0,1]
	v_pk_mul_f32 v[26:27], v[226:227], v[26:27] op_sel_hi:[0,1]
	v_pk_mul_f32 v[24:25], v[226:227], v[24:25] op_sel_hi:[0,1]
	v_pk_mul_f32 v[22:23], v[226:227], v[22:23] op_sel_hi:[0,1]
	v_pk_mul_f32 v[20:21], v[226:227], v[20:21] op_sel_hi:[0,1]
	v_pk_mul_f32 v[18:19], v[226:227], v[18:19] op_sel_hi:[0,1]
	v_pk_mul_f32 v[16:17], v[226:227], v[16:17] op_sel_hi:[0,1]
	v_pk_mul_f32 v[50:51], v[226:227], v[50:51] op_sel_hi:[0,1]
	v_pk_mul_f32 v[48:49], v[226:227], v[48:49] op_sel_hi:[0,1]
	s_branch .Lat_back_L2

.Lat_rare_P17:
	v_mov_b32_e32 v227, v226
	s_nop 1
	v_permlane32_swap_b32_e32 v226, v227
	v_max_f32_e32 v226, v226, v227
	v_max_f32_e32 v226, v226, v226
	v_max_f32_e32 v227, 0, v226
	v_exp_f32_e64 v226, -v227
	v_sub_f32_e32 v127, v127, v227
	v_sub_f32_e32 v126, v126, v227
	v_sub_f32_e32 v125, v125, v227
	v_sub_f32_e32 v124, v124, v227
	v_sub_f32_e32 v123, v123, v227
	v_sub_f32_e32 v122, v122, v227
	v_sub_f32_e32 v121, v121, v227
	v_sub_f32_e32 v120, v120, v227
	v_sub_f32_e32 v119, v119, v227
	v_sub_f32_e32 v118, v118, v227
	v_sub_f32_e32 v117, v117, v227
	v_sub_f32_e32 v116, v116, v227
	v_sub_f32_e32 v115, v115, v227
	v_sub_f32_e32 v114, v114, v227
	v_sub_f32_e32 v113, v113, v227
	v_sub_f32_e32 v112, v112, v227
	v_sub_f32_e32 v79, v79, v227
	v_sub_f32_e32 v78, v78, v227
	v_sub_f32_e32 v77, v77, v227
	v_sub_f32_e32 v76, v76, v227
	v_sub_f32_e32 v75, v75, v227
	v_sub_f32_e32 v74, v74, v227
	v_sub_f32_e32 v73, v73, v227
	v_sub_f32_e32 v72, v72, v227
	v_sub_f32_e32 v71, v71, v227
	v_sub_f32_e32 v70, v70, v227
	v_sub_f32_e32 v69, v69, v227
	v_sub_f32_e32 v68, v68, v227
	v_sub_f32_e32 v67, v67, v227
	v_sub_f32_e32 v66, v66, v227
	v_sub_f32_e32 v65, v65, v227
	v_sub_f32_e32 v64, v64, v227
	v_pk_mul_f32 v[46:47], v[226:227], v[46:47] op_sel_hi:[0,1]
	v_pk_mul_f32 v[44:45], v[226:227], v[44:45] op_sel_hi:[0,1]
	v_pk_mul_f32 v[42:43], v[226:227], v[42:43] op_sel_hi:[0,1]
	v_pk_mul_f32 v[40:41], v[226:227], v[40:41] op_sel_hi:[0,1]
	v_pk_mul_f32 v[38:39], v[226:227], v[38:39] op_sel_hi:[0,1]
	v_pk_mul_f32 v[36:37], v[226:227], v[36:37] op_sel_hi:[0,1]
	v_pk_mul_f32 v[34:35], v[226:227], v[34:35] op_sel_hi:[0,1]
	v_pk_mul_f32 v[32:33], v[226:227], v[32:33] op_sel_hi:[0,1]
	v_pk_mul_f32 v[30:31], v[226:227], v[30:31] op_sel_hi:[0,1]
	v_pk_mul_f32 v[28:29], v[226:227], v[28:29] op_sel_hi:[0,1]
	v_pk_mul_f32 v[26:27], v[226:227], v[26:27] op_sel_hi:[0,1]
	v_pk_mul_f32 v[24:25], v[226:227], v[24:25] op_sel_hi:[0,1]
	v_pk_mul_f32 v[22:23], v[226:227], v[22:23] op_sel_hi:[0,1]
	v_pk_mul_f32 v[20:21], v[226:227], v[20:21] op_sel_hi:[0,1]
	v_pk_mul_f32 v[18:19], v[226:227], v[18:19] op_sel_hi:[0,1]
	v_pk_mul_f32 v[16:17], v[226:227], v[16:17] op_sel_hi:[0,1]
	v_pk_mul_f32 v[50:51], v[226:227], v[50:51] op_sel_hi:[0,1]
	v_pk_mul_f32 v[48:49], v[226:227], v[48:49] op_sel_hi:[0,1]
	s_branch .LBB3_13

	.amdhsa_kernel _Z13attn11_kernelILi4EEvPc
		.amdhsa_group_segment_fixed_size 16384
		.amdhsa_private_segment_fixed_size 0
		.amdhsa_kernarg_size 264
		.amdhsa_user_sgpr_count 2
		.amdhsa_user_sgpr_dispatch_ptr 0
		.amdhsa_user_sgpr_queue_ptr 0
		.amdhsa_user_sgpr_kernarg_segment_ptr 1
		.amdhsa_user_sgpr_dispatch_id 0
		.amdhsa_user_sgpr_kernarg_preload_length 0
		.amdhsa_user_sgpr_kernarg_preload_offset 0
		.amdhsa_user_sgpr_private_segment_size 0
		.amdhsa_uses_dynamic_stack 0
		.amdhsa_enable_private_segment 0
		.amdhsa_system_sgpr_workgroup_id_x 1
		.amdhsa_system_sgpr_workgroup_id_y 0
		.amdhsa_system_sgpr_workgroup_id_z 0
		.amdhsa_system_sgpr_workgroup_info 0
		.amdhsa_system_vgpr_workitem_id 0
		.amdhsa_next_free_vgpr 228
		.amdhsa_next_free_sgpr 56
		.amdhsa_accum_offset 228
		.amdhsa_reserve_vcc 1
		.amdhsa_float_round_mode_32 0
		.amdhsa_float_round_mode_16_64 0
		.amdhsa_float_denorm_mode_32 3
		.amdhsa_float_denorm_mode_16_64 3
		.amdhsa_dx10_clamp 1
		.amdhsa_ieee_mode 1
		.amdhsa_fp16_overflow 0
		.amdhsa_tg_split 0
		.amdhsa_exception_fp_ieee_invalid_op 0
		.amdhsa_exception_fp_denorm_src 0
		.amdhsa_exception_fp_ieee_div_zero 0
		.amdhsa_exception_fp_ieee_overflow 0
		.amdhsa_exception_fp_ieee_underflow 0
		.amdhsa_exception_fp_ieee_inexact 0
		.amdhsa_exception_int_div_zero 0
	.end_amdhsa_kernel

amdhsa.kernels:
  - .agpr_count:     0
    .args:
      - .actual_access:  read_only
        .address_space:  global
        .offset:         0
        .size:           8
        .value_kind:     global_buffer
      - .actual_access:  read_only
        .address_space:  global
        .offset:         8
        .size:           8
        .value_kind:     global_buffer
      - .actual_access:  read_only
        .address_space:  global
        .offset:         16
        .size:           8
        .value_kind:     global_buffer
      - .actual_access:  read_only
        .address_space:  global
        .offset:         24
        .size:           8
        .value_kind:     global_buffer
      - .actual_access:  read_only
        .address_space:  global
        .offset:         32
        .size:           8
        .value_kind:     global_buffer
      - .actual_access:  read_only
        .address_space:  global
        .offset:         40
        .size:           8
        .value_kind:     global_buffer
      - .actual_access:  read_only
        .address_space:  global
        .offset:         48
        .size:           8
        .value_kind:     global_buffer
      - .actual_access:  write_only
        .address_space:  global
        .offset:         56
        .size:           8
        .value_kind:     global_buffer
    .group_segment_fixed_size: 32
    .kernarg_segment_align: 8
    .kernarg_segment_size: 64
    .language:       OpenCL C
    .language_version:
      - 2
      - 0
    .max_flat_workgroup_size: 256
    .name:           _Z11prep_kernelPKfS0_S0_S0_S0_S0_S0_Pc
    .private_segment_fixed_size: 0
    .sgpr_count:     48
    .sgpr_spill_count: 0
    .symbol:         _Z11prep_kernelPKfS0_S0_S0_S0_S0_S0_Pc.kd
    .uniform_work_group_size: 1
    .uses_dynamic_stack: false
    .vgpr_count:     78
    .vgpr_spill_count: 0
    .wavefront_size: 64
  - .agpr_count:     0
    .args:
      - .address_space:  global
        .offset:         0
        .size:           8
        .value_kind:     global_buffer
      - .actual_access:  read_only
        .address_space:  global
        .offset:         8
        .size:           8
        .value_kind:     global_buffer
      - .actual_access:  read_only
        .address_space:  global
        .offset:         16
        .size:           8
        .value_kind:     global_buffer
    .group_segment_fixed_size: 0
    .kernarg_segment_align: 8
    .kernarg_segment_size: 24
    .language:       OpenCL C
    .language_version:
      - 2
      - 0
    .max_flat_workgroup_size: 512
    .name:           _Z13qkv256_kernelPcPKfS1_
    .private_segment_fixed_size: 0
    .sgpr_count:     35
    .sgpr_spill_count: 0
    .symbol:         _Z13qkv256_kernelPcPKfS1_.kd
    .uniform_work_group_size: 1
    .uses_dynamic_stack: false
    .vgpr_count:     214
    .vgpr_spill_count: 0
    .wavefront_size: 64
  - .agpr_count:     0
    .args:
      - .address_space:  global
        .offset:         0
        .size:           8
        .value_kind:     global_buffer
      - .actual_access:  read_only
        .address_space:  global
        .offset:         8
        .size:           8
        .value_kind:     global_buffer
      - .actual_access:  read_only
        .address_space:  global
        .offset:         16
        .size:           8
        .value_kind:     global_buffer
      - .actual_access:  write_only
        .address_space:  global
        .offset:         24
        .size:           8
        .value_kind:     global_buffer
    .group_segment_fixed_size: 0
    .kernarg_segment_align: 8
    .kernarg_segment_size: 32
    .language:       OpenCL C
    .language_version:
      - 2
      - 0
    .max_flat_workgroup_size: 256
    .name:           _Z11proj_kernelPKcPKfS2_Pf
    .private_segment_fixed_size: 0
    .sgpr_count:     34
    .sgpr_spill_count: 0
    .symbol:         _Z11proj_kernelPKcPKfS2_Pf.kd
    .uniform_work_group_size: 1
    .uses_dynamic_stack: false
    .vgpr_count:     185
    .vgpr_spill_count: 0
    .wavefront_size: 64
  - .agpr_count:     0
    .args:
      - .address_space:  global
        .offset:         0
        .size:           8
        .value_kind:     global_buffer
      - .offset:         8
        .size:           4
        .value_kind:     hidden_block_count_x
      - .offset:         12
        .size:           4
        .value_kind:     hidden_block_count_y
      - .offset:         16
        .size:           4
        .value_kind:     hidden_block_count_z
      - .offset:         20
        .size:           2
        .value_kind:     hidden_group_size_x
      - .offset:         22
        .size:           2
        .value_kind:     hidden_group_size_y
      - .offset:         24
        .size:           2
        .value_kind:     hidden_group_size_z
      - .offset:         26
        .size:           2
        .value_kind:     hidden_remainder_x
      - .offset:         28
        .size:           2
        .value_kind:     hidden_remainder_y
      - .offset:         30
        .size:           2
        .value_kind:     hidden_remainder_z
      - .offset:         48
        .size:           8
        .value_kind:     hidden_global_offset_x
      - .offset:         56
        .size:           8
        .value_kind:     hidden_global_offset_y
      - .offset:         64
        .size:           8
        .value_kind:     hidden_global_offset_z
      - .offset:         72
        .size:           2
        .value_kind:     hidden_grid_dims
      - .offset:         128
        .size:           4
        .value_kind:     hidden_dynamic_lds_size
    .group_segment_fixed_size: 16384
    .kernarg_segment_align: 8
    .kernarg_segment_size: 264
    .language:       OpenCL C
    .language_version:
      - 2
      - 0
    .max_flat_workgroup_size: 256
    .name:           _Z13attn11_kernelILi4EEvPc
    .private_segment_fixed_size: 0
    .sgpr_count:     62
    .sgpr_spill_count: 0
    .symbol:         _Z13attn11_kernelILi4EEvPc.kd
    .uniform_work_group_size: 1
    .uses_dynamic_stack: false
    .vgpr_count:     228
    .vgpr_spill_count: 0
    .wavefront_size: 64
